# MP0 stage-3 wave-0-only feature-chunk build: 4 v_cvt_pk_f16_f32 + 4 v_cndmask instead of 8 cvt + 8 cndmask + 4 pack (12 fewer VALU on the pole wave per tile)
# speedup vs baseline: 1.0119x; 1.0078x over previous
.LBB5_14:
	v_or_b32_e32 v0, s33, v200
	ds_read_b128 v[142:145], v0 offset:0
	s_waitcnt lgkmcnt(4)
	s_nop 0
	v_mfma_f32_16x16x32_f16 v[134:137], v[114:117], v[134:137], v[166:169]
	ds_read_b128 v[146:149], v0 offset:0x1000
	s_waitcnt lgkmcnt(4)
	s_nop 0
	v_mfma_f32_16x16x32_f16 v[138:141], v[114:117], v[138:141], v[170:173]
	ds_read_b128 v[150:153], v0 offset:0x2000
	s_waitcnt lgkmcnt(4)
	s_nop 0
	v_mfma_f32_16x16x32_f16 v[154:157], v[114:117], v[158:161], v[174:177]
	ds_read_b128 v[158:161], v0 offset:0x3000
	s_waitcnt lgkmcnt(4)
	s_nop 0
	v_mfma_f32_16x16x32_f16 v[162:165], v[114:117], v[162:165], v[178:181]
	ds_read_b128 v[166:169], v205 offset:0
	s_waitcnt lgkmcnt(4)
	s_nop 0
	v_mfma_f32_16x16x32_f16 v[134:137], v[106:109], v[142:145], v[134:137]
	ds_read_b128 v[142:145], v205 offset:0x100
	s_waitcnt lgkmcnt(4)
	s_nop 0
	v_mfma_f32_16x16x32_f16 v[138:141], v[106:109], v[146:149], v[138:141]
	ds_read_b128 v[146:149], v205 offset:0x200
	s_waitcnt lgkmcnt(4)
	s_nop 0
	v_mfma_f32_16x16x32_f16 v[150:153], v[106:109], v[150:153], v[154:157]
	ds_read_b128 v[154:157], v205 offset:0x300
	s_waitcnt lgkmcnt(4)
	s_nop 0
	v_mfma_f32_16x16x32_f16 v[158:161], v[106:109], v[158:161], v[162:165]
	s_waitcnt lgkmcnt(3)
	s_nop 0
	v_mfma_f32_16x16x32_f16 v[134:137], v[102:105], v[166:169], v[134:137]
	s_waitcnt lgkmcnt(2)
	s_nop 0
	v_mfma_f32_16x16x32_f16 v[138:141], v[102:105], v[142:145], v[138:141]
	s_waitcnt lgkmcnt(1)
	s_nop 0
	v_mfma_f32_16x16x32_f16 v[142:145], v[102:105], v[146:149], v[150:153]
	s_waitcnt lgkmcnt(0)
	s_nop 0
	v_mfma_f32_16x16x32_f16 v[146:149], v[102:105], v[154:157], v[158:161]
	s_nop 1
	v_cvt_pk_f16_f32 v1, v136, v137
	v_pk_max_f16 v1, v1, 0
	v_cvt_pk_f16_f32 v0, v134, v135
	v_pk_max_f16 v0, v0, 0
	v_cvt_pk_f16_f32 v135, v140, v141
	v_pk_max_f16 v135, v135, 0
	v_cvt_pk_f16_f32 v134, v138, v139
	v_pk_max_f16 v134, v134, 0
	ds_write2st64_b64 v218, v[0:1], v[134:135] offset1:8
	v_cvt_pk_f16_f32 v1, v144, v145
	v_pk_max_f16 v1, v1, 0
	v_cvt_pk_f16_f32 v0, v142, v143
	v_pk_max_f16 v0, v0, 0
	s_lshl_b32 s34, s2, 14
	v_cvt_pk_f16_f32 v135, v148, v149
	v_pk_max_f16 v135, v135, 0
	v_cvt_pk_f16_f32 v134, v146, v147
	v_pk_max_f16 v134, v134, 0
	s_or_b32 s34, s34, 0x18000
	ds_write2st64_b64 v218, v[0:1], v[134:135] offset0:16 offset1:24
	v_or_b32_e32 v172, s34, v197
	v_or_b32_e32 v223, s34, v198
	v_or_b32_e32 v143, s34, v199
	v_or_b32_e32 v142, s34, v200
	v_add_u32_e32 v0, s34, v208
	s_xor_b32 s34, s2, 1
	s_waitcnt vmcnt(2) lgkmcnt(0)
	s_barrier
	ds_read_b128 v[134:137], v201 offset:0
	s_mul_i32 s37, s34, 0xc000
	ds_read_b128 v[138:141], v202 offset:0
	ds_read_b128 v[144:147], v203 offset:0
	ds_read_b128 v[148:151], v204 offset:0
	v_add_u32_e32 v1, s37, v209
	ds_read_b128 v[152:155], v1 offset:0
	ds_read_b128 v[156:159], v1 offset:0x4000
	ds_read_b128 v[160:163], v1 offset:0x8000
	ds_read_b128 v[164:167], v1 offset:0x400
	ds_read_b128 v[168:171], v1 offset:0x4400
	ds_read_b128 v[174:177], v1 offset:0x8400
	ds_read_b128 v[178:181], v172 offset:0
	s_waitcnt lgkmcnt(10)
	v_subrev_u32_e32 v186, 56, v215
	v_mfma_f32_16x16x32_f16 v[182:185], v[2:5], v[134:137], v[118:121]
	v_min_u32_e32 v225, s17, v186
	v_add_u32_e32 v224, s20, v216
	v_mov_b32_e32 v230, s16
	v_mfma_f32_16x16x32_f16 v[186:189], v[42:45], v[134:137], v[122:125]
	v_cmp_gt_u32_e32 vcc, s8, v224
	ds_read_b128 v[226:229], v223 offset:0
	s_waitcnt lgkmcnt(10)
	v_mfma_f32_16x16x32_f16 v[134:137], v[66:69], v[134:137], v[126:129]
	v_lshl_or_b32 v173, v196, 8, v190
	v_cndmask_b32_e32 v230, v230, v224, vcc
	v_lshlrev_b32_e32 v234, 5, v230
	v_mfma_f32_16x16x32_f16 v[182:185], v[6:9], v[138:141], v[182:185]
	v_add_u32_e32 v196, -8, v215
	v_min_u32_e32 v238, s17, v196
	v_subrev_u32_e32 v196, 52, v215
	v_mfma_f32_16x16x32_f16 v[186:189], v[46:49], v[138:141], v[186:189]
	v_add_u32_e32 v221, -4, v215
	v_min_u32_e32 v196, s18, v196
	v_min_u32_e32 v221, s18, v221
	v_mfma_f32_16x16x32_f16 v[230:233], v[70:73], v[138:141], v[134:137]
	global_load_dwordx4 v[134:137], v234, s[6:7]
	global_load_dwordx4 v[138:141], v234, s[6:7] offset:16
	ds_read_b128 v[234:237], v143 offset:0
	s_waitcnt lgkmcnt(10)
	v_lshl_or_b32 v242, v192, 8, v190
	v_mfma_f32_16x16x32_f16 v[182:185], v[50:53], v[144:147], v[182:185]
	global_load_dword v192, v196, s[4:5]
	v_subrev_u32_e32 v239, 48, v215
	global_load_dword v221, v221, s[4:5]
	v_mfma_f32_16x16x32_f16 v[186:189], v[18:21], v[144:147], v[186:189]
	v_min_u32_e32 v222, s19, v215
	v_min_u32_e32 v239, s19, v239
	v_lshl_or_b32 v241, v194, 8, v191
	v_mfma_f32_16x16x32_f16 v[144:147], v[74:77], v[144:147], v[230:233]
	global_load_dword v196, v239, s[4:5]
	ds_read_b128 v[230:233], v142 offset:0
	s_waitcnt lgkmcnt(10)
	global_load_dword v194, v222, s[4:5]
	s_add_i32 s2, s28, s3
	v_mfma_f32_16x16x32_f16 v[182:185], v[10:13], v[148:151], v[182:185]
	v_lshl_or_b32 v243, v193, 8, v190
	global_load_dword v193, v225, s[4:5]
	s_min_i32 s35, s2, s14
	v_mfma_f32_16x16x32_f16 v[186:189], v[58:61], v[148:151], v[186:189]
	global_load_dword v222, v238, s[4:5]
	s_lshl_b32 s35, s35, 14
	s_lshl_b32 s34, s34, 14
	v_mfma_f32_16x16x32_f16 v[148:151], v[90:93], v[148:151], v[144:147]
	s_add_i32 s36, s33, 0
	v_add_u32_e32 v1, s35, v210
	s_add_i32 s38, s25, s34
	s_add_i32 s39, s36, s21
	s_add_i32 s40, s26, s34
	s_add_i32 s34, s36, s23
	s_add_i32 m0, s39, 0x8000
	v_add_u32_e32 v240, s35, v211
	s_add_i32 s41, s34, 0x8000
	s_add_i32 s35, s39, 0x4000
	s_add_i32 s36, s22, s33
	v_add_u32_e32 v239, s37, v212
	ds_read_b128 v[144:147], v201 offset:0x1000
	s_waitcnt lgkmcnt(4)
	s_waitcnt lgkmcnt(5)
	s_nop 0
	v_pk_add_f16 v152, v152, v156
	v_pk_add_f16 v153, v153, v157
	v_pk_add_f16 v154, v154, v158
	v_pk_add_f16 v155, v155, v159
	v_pk_add_f16 v154, v154, v162
	v_pk_add_f16 v155, v155, v163
	v_pk_add_f16 v153, v153, v161
	v_pk_add_f16 v152, v152, v160
	ds_write_b128 v239, v[152:155]
	v_pk_add_f16 v152, v164, v168
	v_pk_add_f16 v153, v165, v169
	v_pk_add_f16 v154, v166, v170
	v_pk_add_f16 v155, v167, v171
	v_pk_add_f16 v154, v154, v176
	v_pk_add_f16 v155, v155, v177
	v_pk_add_f16 v153, v153, v175
	v_pk_add_f16 v152, v152, v174
	ds_write_b128 v239, v[152:155] offset:1024
	ds_read_b128 v[152:155], v202 offset:0x1000
	s_waitcnt lgkmcnt(4)
	global_load_lds_dwordx4 v173, s[12:13]
	s_mov_b32 m0, s38
	ds_read_b128 v[168:171], v203 offset:0x1000
	s_waitcnt lgkmcnt(4)
	v_mfma_f32_16x16x32_f16 v[182:185], v[14:17], v[178:181], v[182:185]
	global_load_lds_dwordx4 v1, s[12:13]
	ds_read_b128 v[174:177], v204 offset:0x1000
	v_mfma_f32_16x16x32_f16 v[186:189], v[22:25], v[178:181], v[186:189]
	s_waitcnt lgkmcnt(4)
	v_mfma_f32_16x16x32_f16 v[178:181], v[86:89], v[178:181], v[130:133]
	v_mfma_f32_16x16x32_f16 v[156:159], v[26:29], v[226:229], v[182:185]
	v_mfma_f32_16x16x32_f16 v[160:163], v[34:37], v[226:229], v[186:189]
	v_mfma_f32_16x16x32_f16 v[164:167], v[78:81], v[226:229], v[178:181]
	v_mfma_f32_16x16x32_f16 v[156:159], v[30:33], v[234:237], v[156:159]
	v_mfma_f32_16x16x32_f16 v[160:163], v[38:41], v[234:237], v[160:163]
	v_mfma_f32_16x16x32_f16 v[164:167], v[82:85], v[234:237], v[164:167]
	v_mfma_f32_16x16x32_f16 v[156:159], v[54:57], v[230:233], v[156:159]
	v_mfma_f32_16x16x32_f16 v[160:163], v[62:65], v[230:233], v[160:163]
	v_mfma_f32_16x16x32_f16 v[164:167], v[94:97], v[230:233], v[164:167]
	s_mov_b32 m0, s41
	ds_read_b64 v[234:235], v0 offset:0
	ds_read_b128 v[178:181], v172 offset:0x1000
	s_waitcnt lgkmcnt(5)
	ds_read_b128 v[186:189], v223 offset:0x1000
	s_waitcnt lgkmcnt(5)
	s_nop 4
	v_exp_f32_e32 v1, v156
	s_waitcnt lgkmcnt(2)
	ds_read_b128 v[230:233], v143 offset:0x1000
	s_waitcnt lgkmcnt(5)
	global_load_lds_dwordx4 v241, s[12:13]
	v_add_f32_e32 v1, 1.0, v1
	v_rcp_f32_e32 v1, v1
	v_exp_f32_e32 v156, v160
	v_mfma_f32_16x16x32_f16 v[182:185], v[2:5], v[144:147], v[118:121]
	v_add_u32_e32 v225, v206, v213
	v_fma_f32 v1, v1, v164, v148
	v_exp_f32_e32 v1, v1
	v_add_f32_e32 v148, 1.0, v156
	v_exp_f32_e32 v156, v157
	v_rcp_f32_e32 v148, v148
	v_add_f32_e32 v1, 1.0, v1
	v_rcp_f32_e32 v1, v1
	v_add_f32_e32 v156, 1.0, v156
	v_rcp_f32_e32 v156, v156
	v_mfma_f32_16x16x32_f16 v[226:229], v[42:45], v[144:147], v[122:125]
	v_fma_f32 v1, v1, -2.0, 1.0
	v_fma_f32 v1, -v148, v1, v1
	v_fma_mixlo_f16 v1, v148, v234, v1 op_sel_hi:[0,1,0]
	v_mfma_f32_16x16x32_f16 v[144:147], v[66:69], v[144:147], v[126:129]
	v_exp_f32_e32 v148, v161
	v_fma_f32 v149, v156, v165, v149
	v_exp_f32_e32 v149, v149
	v_mfma_f32_16x16x32_f16 v[182:185], v[6:9], v[152:155], v[182:185]
	v_add_f32_e32 v148, 1.0, v148
	v_rcp_f32_e32 v156, v148
	v_add_f32_e32 v148, 1.0, v149
	v_mfma_f32_16x16x32_f16 v[226:229], v[46:49], v[152:155], v[226:229]
	v_rcp_f32_e32 v157, v148
	v_add_u32_e32 v173, 0x1000, v225
	v_mfma_f32_16x16x32_f16 v[144:147], v[70:73], v[152:155], v[144:147]
	v_mfma_f32_16x16x32_f16 v[152:155], v[50:53], v[168:171], v[182:185]
	v_mfma_f32_16x16x32_f16 v[182:185], v[18:21], v[168:171], v[226:229]
	v_mfma_f32_16x16x32_f16 v[144:147], v[74:77], v[168:171], v[144:147]
	ds_read_b128 v[168:171], v142 offset:0x1000
	s_waitcnt lgkmcnt(5)
	s_nop 0
	v_mfma_f32_16x16x32_f16 v[152:155], v[10:13], v[174:177], v[152:155]
	v_mfma_f32_16x16x32_f16 v[182:185], v[58:61], v[174:177], v[182:185]
	v_mfma_f32_16x16x32_f16 v[146:149], v[90:93], v[174:177], v[144:147]
	s_nop 3
	v_fma_f32 v144, v157, -2.0, 1.0
	v_fma_f32 v144, -v156, v144, v144
	v_fma_mixlo_f16 v144, v156, v234, v144 op_sel:[0,1,0] op_sel_hi:[0,1,0]
	s_mov_b32 m0, s40
	ds_read_b128 v[174:177], v201 offset:0x2000
	s_waitcnt lgkmcnt(4)
	ds_read_b128 v[226:229], v202 offset:0x2000
	s_waitcnt lgkmcnt(4)
	v_exp_f32_e32 v145, v158
	global_load_lds_dwordx4 v240, s[12:13]
	v_exp_f32_e32 v156, v162
	v_add_f32_e32 v145, 1.0, v145
	v_rcp_f32_e32 v145, v145
	v_mfma_f32_16x16x32_f16 v[152:155], v[14:17], v[178:181], v[152:155]
	v_pack_b32_f16 v144, v1, v144
	v_fma_f32 v145, v145, v166, v150
	v_add_f32_e32 v150, 1.0, v156
	v_rcp_f32_e32 v234, v150
	v_exp_f32_e32 v150, v159
	v_mfma_f32_16x16x32_f16 v[182:185], v[22:25], v[178:181], v[182:185]
	v_exp_f32_e32 v145, v145
	v_add_f32_e32 v150, 1.0, v150
	v_mfma_f32_16x16x32_f16 v[178:181], v[86:89], v[178:181], v[130:133]
	v_rcp_f32_e32 v150, v150
	v_add_f32_e32 v145, 1.0, v145
	v_rcp_f32_e32 v145, v145
	v_mfma_f32_16x16x32_f16 v[182:185], v[34:37], v[186:189], v[182:185]
	v_fmac_f32_e32 v151, v150, v167
	v_fma_f32 v145, v145, -2.0, 1.0
	v_mfma_f32_16x16x32_f16 v[178:181], v[78:81], v[186:189], v[178:181]
	v_fma_f32 v145, -v234, v145, v145
	v_fma_mixlo_f16 v145, v234, v235, v145 op_sel_hi:[0,1,0]
	v_mfma_f32_16x16x32_f16 v[152:155], v[26:29], v[186:189], v[152:155]
	ds_read_b128 v[186:189], v203 offset:0x2000
	s_waitcnt lgkmcnt(4)
	ds_read_b128 v[164:167], v204 offset:0x2000
	s_waitcnt lgkmcnt(4)
	s_nop 0
	v_mfma_f32_16x16x32_f16 v[156:159], v[38:41], v[230:233], v[182:185]
	s_nop 2
	v_exp_f32_e32 v182, v163
	v_mfma_f32_16x16x32_f16 v[160:163], v[82:85], v[230:233], v[178:181]
	s_nop 2
	v_exp_f32_e32 v178, v151
	v_mfma_f32_16x16x32_f16 v[152:155], v[30:33], v[230:233], v[152:155]
	v_add_f32_e32 v179, 1.0, v182
	v_add_f32_e32 v178, 1.0, v178
	v_mfma_f32_16x16x32_f16 v[150:153], v[54:57], v[168:171], v[152:155]
	v_mfma_f32_16x16x32_f16 v[154:157], v[62:65], v[168:171], v[156:159]
	s_nop 2
	v_rcp_f32_e32 v158, v178
	v_rcp_f32_e32 v159, v179
	v_mfma_f32_16x16x32_f16 v[168:171], v[94:97], v[168:171], v[160:163]
	v_fma_f32 v158, v158, -2.0, 1.0
	v_fma_f32 v158, -v159, v158, v158
	v_fma_mixlo_f16 v158, v159, v235, v158 op_sel:[0,1,0] op_sel_hi:[0,1,0]
	s_nop 0
	v_pack_b32_f16 v145, v145, v158
	global_store_dwordx2 v173, v[144:145], s[0:1] nt
	s_mov_b32 m0, s36
	ds_read_b64 v[238:239], v0 offset:0x1000
	ds_read_b128 v[178:181], v172 offset:0x2000
	s_waitcnt lgkmcnt(5)
	ds_read_b128 v[182:185], v223 offset:0x2000
	s_waitcnt lgkmcnt(5)
	v_exp_f32_e32 v1, v150
	s_waitcnt lgkmcnt(2)
	ds_read_b128 v[234:237], v143 offset:0x2000
	s_waitcnt lgkmcnt(5)
	global_load_lds_dwordx4 v243, s[12:13]
	v_add_f32_e32 v1, 1.0, v1
	v_rcp_f32_e32 v1, v1
	v_exp_f32_e32 v145, v151
	v_mfma_f32_16x16x32_f16 v[158:161], v[2:5], v[174:177], v[118:121]
	v_exp_f32_e32 v144, v154
	v_fma_f32 v1, v1, v168, v146
	v_exp_f32_e32 v1, v1
	v_mfma_f32_16x16x32_f16 v[230:233], v[42:45], v[174:177], v[122:125]
	v_add_f32_e32 v145, 1.0, v145
	v_rcp_f32_e32 v145, v145
	v_add_f32_e32 v1, 1.0, v1
	v_mfma_f32_16x16x32_f16 v[174:177], v[66:69], v[174:177], v[126:129]
	v_add_f32_e32 v144, 1.0, v144
	v_rcp_f32_e32 v1, v1
	v_rcp_f32_e32 v144, v144
	v_mfma_f32_16x16x32_f16 v[158:161], v[6:9], v[226:229], v[158:161]
	v_fma_f32 v145, v145, v169, v147
	v_exp_f32_e32 v145, v145
	v_exp_f32_e32 v146, v155
	v_mfma_f32_16x16x32_f16 v[174:177], v[70:73], v[226:229], v[174:177]
	v_fma_f32 v1, v1, -2.0, 1.0
	v_fma_f32 v1, -v144, v1, v1
	v_fma_mixlo_f16 v240, v144, v238, v1 op_sel_hi:[0,1,0]
	v_mfma_f32_16x16x32_f16 v[230:233], v[46:49], v[226:229], v[230:233]
	v_add_f32_e32 v144, 1.0, v145
	v_add_f32_e32 v1, 1.0, v146
	v_rcp_f32_e32 v150, v144
	v_mfma_f32_16x16x32_f16 v[158:161], v[50:53], v[186:189], v[158:161]
	v_rcp_f32_e32 v1, v1
	v_add_u32_e32 v173, 0x2000, v225
	v_fma_f32 v150, v150, -2.0, 1.0
	v_mfma_f32_16x16x32_f16 v[174:177], v[74:77], v[186:189], v[174:177]
	v_fma_f32 v243, -v1, v150, v150
	v_mfma_f32_16x16x32_f16 v[226:229], v[18:21], v[186:189], v[230:233]
	ds_read_b128 v[186:189], v142 offset:0x2000
	s_waitcnt lgkmcnt(5)
	s_nop 0
	v_mfma_f32_16x16x32_f16 v[158:161], v[10:13], v[164:167], v[158:161]
	v_mfma_f32_16x16x32_f16 v[144:147], v[90:93], v[164:167], v[174:177]
	v_mfma_f32_16x16x32_f16 v[226:229], v[58:61], v[164:167], v[226:229]
	s_mov_b32 m0, s35
	ds_read_b128 v[230:233], v201 offset:0x3000
	s_waitcnt lgkmcnt(4)
	v_exp_f32_e32 v150, v152
	v_mfma_f32_16x16x32_f16 v[164:167], v[14:17], v[178:181], v[158:161]
	ds_read_b128 v[160:163], v202 offset:0x3000
	s_waitcnt lgkmcnt(4)
	global_load_lds_dwordx4 v242, s[12:13]
	v_exp_f32_e32 v154, v153
	v_add_f32_e32 v150, 1.0, v150
	v_rcp_f32_e32 v150, v150
	v_mfma_f32_16x16x32_f16 v[174:177], v[22:25], v[178:181], v[226:229]
	v_add_f32_e32 v154, 1.0, v154
	v_rcp_f32_e32 v154, v154
	v_exp_f32_e32 v151, v156
	v_mfma_f32_16x16x32_f16 v[178:181], v[86:89], v[178:181], v[130:133]
	v_fma_f32 v148, v150, v170, v148
	v_exp_f32_e32 v148, v148
	v_fmac_f32_e32 v149, v154, v171
	v_mfma_f32_16x16x32_f16 v[226:229], v[26:29], v[182:185], v[164:167]
	v_exp_f32_e32 v149, v149
	v_add_f32_e32 v150, 1.0, v151
	v_rcp_f32_e32 v241, v150
	v_mfma_f32_16x16x32_f16 v[174:177], v[34:37], v[182:185], v[174:177]
	v_add_f32_e32 v148, 1.0, v148
	ds_read_b128 v[164:167], v203 offset:0x3000
	s_waitcnt lgkmcnt(4)
	v_mfma_f32_16x16x32_f16 v[178:181], v[78:81], v[182:185], v[178:181]
	v_exp_f32_e32 v155, v157
	v_rcp_f32_e32 v148, v148
	v_add_f32_e32 v149, 1.0, v149
	v_mfma_f32_16x16x32_f16 v[150:153], v[30:33], v[234:237], v[226:229]
	v_rcp_f32_e32 v149, v149
	ds_read_b128 v[168:171], v204 offset:0x3000
	s_waitcnt lgkmcnt(4)
	v_mfma_f32_16x16x32_f16 v[174:177], v[38:41], v[234:237], v[174:177]
	v_fma_f32 v148, v148, -2.0, 1.0
	v_fma_f32 v148, -v241, v148, v148
	v_fma_mixlo_f16 v241, v241, v239, v148 op_sel_hi:[0,1,0]
	v_mfma_f32_16x16x32_f16 v[178:181], v[82:85], v[234:237], v[178:181]
	v_fma_mixhi_f16 v240, v1, v238, v243 op_sel:[0,1,0] op_sel_hi:[0,1,0]
	v_mfma_f32_16x16x32_f16 v[156:159], v[54:57], v[186:189], v[150:153]
	s_nop 2
	v_add_f32_e32 v150, 1.0, v155
	v_mfma_f32_16x16x32_f16 v[152:155], v[62:65], v[186:189], v[174:177]
	s_nop 2
	v_rcp_f32_e32 v174, v150
	v_fma_f32 v175, v149, -2.0, 1.0
	v_mfma_f32_16x16x32_f16 v[148:151], v[94:97], v[186:189], v[178:181]
	v_fma_f32 v175, -v174, v175, v175
	v_fma_mixhi_f16 v241, v174, v239, v175 op_sel:[0,1,0] op_sel_hi:[0,1,0]
	global_store_dwordx2 v173, v[240:241], s[0:1] nt
	ds_read_b64 v[188:189], v0 offset:0x2000
	ds_read_b64 v[0:1], v0 offset:0x3000
	ds_read_b128 v[172:175], v172 offset:0x3000
	s_waitcnt lgkmcnt(6)
	s_andn2_b64 vcc, exec, s[10:11]
	v_mfma_f32_16x16x32_f16 v[180:183], v[2:5], v[230:233], v[118:121]
	s_waitcnt vmcnt(14)
	v_mfma_f32_16x16x32_f16 v[176:179], v[42:45], v[230:233], v[122:125]
	v_mfma_f32_16x16x32_f16 v[184:187], v[66:69], v[230:233], v[126:129]
	s_cbranch_vccnz .LBB5_11
	v_cvt_pk_f16_f32 v226, v134, v135
	v_cvt_pk_f16_f32 v227, v136, v137
	v_cvt_pk_f16_f32 v228, v138, v139
	v_cvt_pk_f16_f32 v229, v140, v141
	v_cmp_gt_i32_e32 vcc, s8, v224
	s_nop 1
	v_cndmask_b32_e32 v226, 0, v226, vcc
	v_cndmask_b32_e32 v227, 0, v227, vcc
	v_cndmask_b32_e32 v228, 0, v228, vcc
	v_cndmask_b32_e32 v229, 0, v229, vcc
	ds_write_b128 v220, v[226:229]
	s_branch .LBB5_11
